# diff16 tile loop: next tile's scalar set-up (buffer parities, DMA target, K read base, K pointer advance) moved from in front of the barrier into the tail of the P.V MFMA stream
# speedup vs baseline: 1.0303x; 1.0043x over previous
; #define SBAR() __builtin_amdgcn_sched_barrier(0)
; #define ELOADV(kt) do { const char* vb_ = (const char*)Vh + (size_t)(kt) * (64 * LDV * 2); sv0 = *(const bf16x8*)(vb_ + voff0); sv1 = *(const bf16x8*)(vb_ + voff1); sv2 = *(const bf16x8*)(vb_ + voff0 + 256); sv3 = *(const bf16x8*)(vb_ + voff1 + 256); } while (0)
; #define ELOADK(kt) do { const char* kb_ = (const char*)Kh + (size_t)(kt) * (64 * LDK * 2); sk0 = *(const bf16x8*)(kb_ + koff0); sk1 = *(const bf16x8*)(kb_ + koff1); } while (0)
; #define EWRITEV(b) do { char* d_ = V_lds + (b) * D16_V; *(bf16x8*)(d_ + vst0) = sv0; *(bf16x8*)(d_ + vst1) = sv1; *(bf16x8*)(d_ + 8 * VP16 + vst0) = sv2; *(bf16x8*)(d_ + 8 * VP16 + vst1) = sv3; } while (0)
; #define EWRITEK(b) do { char* d_ = K_lds + (b) * PB_K; *(bf16x8*)(d_ + KSWZ(sr, sc * 2)) = sk0; *(bf16x8*)(d_ + KSWZ(32 + sr, sc * 2)) = sk1; } while (0)
; template <int LDQ, int LDK, int LDV, int LDO, int DMX> ...
;     ...
;     __syncthreads();
;     bf16x8 pp[2]; { const char* d_ = P_oth + (t & 1) * (4 * PB_P); pp[0] = *(const bf16x8*)(d_); pp[1] = *(const bf16x8*)(d_ + 1024); }
;     const bf16x8 pc[2] = {po[0], po[1]};
;     const bool more = t + 1 < NT;
;     if (more) EQK((t + 1) & 1);
;     const int vb = vlane + (t & 1) * (int)D16_V, vbo = vb + ch * 1024, vbp = vb + (1 - ch) * 1024;
;     SBAR(); pv16d<0>(o, vbo, vbp, pc, pp); SBAR();
;     asm volatile("s_waitcnt vmcnt(0)" ::: "memory");
;     if (t + 2 < NT) EWRITEK(t & 1);
;     if (t + 1 < NT) EWRITEV((t + 1) & 1);
;     ELOADK(t + 3); ELOADV(t + 2);
;     SBAR(); pv16d<4>(o, vbo, vbp, pc, pp); SBAR();
.Lvd_entry:
	s_add_i32 s60, s55, -1
	s_and_b32 s57, s60, 1
	s_bitcmp1_b32 s55, 0
	s_cselect_b64 s[22:23], -1, 0
	s_and_b64 s[58:59], s[22:23], exec
	s_cselect_b32 s58, 0x4400, 0
	s_cselect_b32 s85, 0x8200, 0
	s_add_i32 s85, s85, s84
	v_add_u32_e32 v178, s58, v193
	s_nop 0
	s_nop 0
	s_nop 0
	s_nop 0
	s_nop 0
.LBB0_1271:
	s_waitcnt vmcnt(2) lgkmcnt(0)
	s_barrier
	ds_read_b128 v[132:135], v178
	ds_read_b128 v[136:139], v178 offset:64
	ds_read_b128 v[144:147], v178 offset:4352
	ds_read_b128 v[148:151], v178 offset:4416
	s_mov_b32 m0, s85
	s_nop 0
	global_load_lds_dwordx4 v253, s[74:75]
	s_add_i32 m0, s85, 0x800
	s_nop 0
	global_load_lds_dwordx4 v253, s[74:75] offset:32
	s_add_i32 m0, s85, 0x400
	s_nop 0
	global_load_lds_dwordx4 v253, s[76:77]
	s_add_i32 m0, s85, 0xc00
	s_nop 0
	global_load_lds_dwordx4 v253, s[76:77] offset:32
	s_add_u32 s74, s74, 0xc0000
	s_addc_u32 s75, s75, 0
	s_add_u32 s76, s76, 0xc0000
	s_addc_u32 s77, s77, 0
	s_waitcnt lgkmcnt(3)
	v_mfma_f32_16x16x32_bf16 v[140:143], v[132:135], v[4:7], v[248:251]
	s_mul_i32 s58, s57, 0x8200
	v_mfma_f32_16x16x32_bf16 v[132:135], v[132:135], v[20:23], v[248:251]
	s_waitcnt lgkmcnt(1)
	v_mfma_f32_16x16x32_bf16 v[152:155], v[144:147], v[4:7], v[248:251]
	v_mfma_f32_16x16x32_bf16 v[144:147], v[144:147], v[20:23], v[248:251]
	v_mfma_f32_16x16x32_bf16 v[140:143], v[136:139], v[8:11], v[140:143]
	v_mfma_f32_16x16x32_bf16 v[132:135], v[136:139], v[24:27], v[132:135]
	s_waitcnt lgkmcnt(0)
	v_mfma_f32_16x16x32_bf16 v[136:139], v[148:151], v[8:11], v[152:155]
	v_mfma_f32_16x16x32_bf16 v[144:147], v[148:151], v[24:27], v[144:147]
	ds_read_b128 v[148:151], v178 offset:128
	s_nop 0
	ds_read_b128 v[152:155], v178 offset:192
	s_waitcnt lgkmcnt(1)
	v_mfma_f32_16x16x32_bf16 v[140:143], v[148:151], v[12:15], v[140:143]
	v_mfma_f32_16x16x32_bf16 v[132:135], v[148:151], v[28:31], v[132:135]
	ds_read_b128 v[148:151], v178 offset:4480
	ds_read_b128 v[180:183], v178 offset:4544
	s_waitcnt lgkmcnt(1)
	v_mfma_f32_16x16x32_bf16 v[136:139], v[148:151], v[12:15], v[136:139]
	v_mfma_f32_16x16x32_bf16 v[204:207], v[148:151], v[28:31], v[144:147]
	v_mfma_f32_16x16x32_bf16 v[144:147], v[152:155], v[16:19], v[140:143]
	v_mfma_f32_16x16x32_bf16 v[140:143], v[152:155], v[32:35], v[132:135]
	s_nop 2
	v_lshl_add_u32 v132, s57, 14, v191
	ds_read_b128 v[148:151], v132
	ds_read_b128 v[152:155], v132 offset:1024
	v_add_u32_e32 v132, s58, v194
	s_waitcnt lgkmcnt(2)
	v_mfma_f32_16x16x32_bf16 v[136:139], v[180:183], v[16:19], v[136:139]
	v_add_u32_e32 v179, v132, v195
	v_add_u32_e32 v178, v132, v196
	v_mfma_f32_16x16x32_bf16 v[132:135], v[180:183], v[32:35], v[204:207]
	ds_read_b64_tr_b16 v[180:181], v179 offset:0
	ds_read_b64_tr_b16 v[182:183], v179 offset:0x200
	ds_read_b64_tr_b16 v[204:205], v178 offset:0
	ds_read_b64_tr_b16 v[206:207], v178 offset:0x200
	ds_read_b64_tr_b16 v[208:209], v179 offset:0x820
	ds_read_b64_tr_b16 v[210:211], v179 offset:0xa20
	ds_read_b64_tr_b16 v[212:213], v178 offset:0x820
	ds_read_b64_tr_b16 v[214:215], v178 offset:0xa20
	ds_read_b64_tr_b16 v[216:217], v179 offset:0x1040
	ds_read_b64_tr_b16 v[218:219], v179 offset:0x1240
	ds_read_b64_tr_b16 v[220:221], v178 offset:0x1040
	ds_read_b64_tr_b16 v[222:223], v178 offset:0x1240
	s_waitcnt lgkmcnt(4)
	s_nop 0
	v_mfma_f32_16x16x32_bf16 v[128:131], v[180:183], v[64:67], v[128:131]
	v_mfma_f32_16x16x32_bf16 v[124:127], v[180:183], v[68:71], v[124:127]
	v_mfma_f32_16x16x32_bf16 v[120:123], v[208:211], v[64:67], v[120:123]
	v_mfma_f32_16x16x32_bf16 v[112:115], v[208:211], v[68:71], v[112:115]
	s_waitcnt lgkmcnt(1)
	v_mfma_f32_16x16x32_bf16 v[128:131], v[204:207], v[148:151], v[128:131]
	s_waitcnt lgkmcnt(0)
	v_mfma_f32_16x16x32_bf16 v[124:127], v[204:207], v[152:155], v[124:127]
	v_mfma_f32_16x16x32_bf16 v[120:123], v[212:215], v[148:151], v[120:123]
	v_mfma_f32_16x16x32_bf16 v[112:115], v[212:215], v[152:155], v[112:115]
	ds_read_b64_tr_b16 v[180:181], v179 offset:0x1860
	ds_read_b64_tr_b16 v[182:183], v179 offset:0x1a60
	ds_read_b64_tr_b16 v[204:205], v178 offset:0x1860
	ds_read_b64_tr_b16 v[206:207], v178 offset:0x1a60
	s_waitcnt lgkmcnt(4)
	v_mfma_f32_16x16x32_bf16 v[108:111], v[216:219], v[64:67], v[108:111]
	s_waitcnt lgkmcnt(0)
	ds_read_b64_tr_b16 v[36:37], v179 offset:0x2080
	ds_read_b64_tr_b16 v[38:39], v179 offset:0x2280
	ds_read_b64_tr_b16 v[40:41], v178 offset:0x2080
	ds_read_b64_tr_b16 v[42:43], v178 offset:0x2280
	ds_read_b64_tr_b16 v[44:45], v179 offset:0x28a0
	ds_read_b64_tr_b16 v[46:47], v179 offset:0x2aa0
	ds_read_b64_tr_b16 v[48:49], v178 offset:0x28a0
	ds_read_b64_tr_b16 v[50:51], v178 offset:0x2aa0
	ds_read_b64_tr_b16 v[232:233], v179 offset:0x30c0
	ds_read_b64_tr_b16 v[234:235], v179 offset:0x32c0
	ds_read_b64_tr_b16 v[236:237], v178 offset:0x30c0
	ds_read_b64_tr_b16 v[238:239], v178 offset:0x32c0
	v_mfma_f32_16x16x32_bf16 v[116:119], v[216:219], v[68:71], v[116:119]
	v_mfma_f32_16x16x32_bf16 v[108:111], v[220:223], v[148:151], v[108:111]
	v_mfma_f32_16x16x32_bf16 v[116:119], v[220:223], v[152:155], v[116:119]
	v_mfma_f32_16x16x32_bf16 v[100:103], v[180:183], v[64:67], v[100:103]
	v_mfma_f32_16x16x32_bf16 v[104:107], v[180:183], v[68:71], v[104:107]
	v_mfma_f32_16x16x32_bf16 v[100:103], v[204:207], v[148:151], v[100:103]
	v_mfma_f32_16x16x32_bf16 v[104:107], v[204:207], v[152:155], v[104:107]
	s_waitcnt vmcnt(4)
	s_cmpk_gt_u32 s60, 0x101
	s_cbranch_scc1 .Lvd_kskip
	s_mulk_i32 s57, 0x4400
	v_add_u32_e32 v244, s57, v198
	s_nop 0
	ds_write_b128 v244, v[52:55]
	ds_write_b128 v244, v[56:59] offset:8704
; #define SBAR() __builtin_amdgcn_sched_barrier(0)
; #define ELOADV(kt) do { const char* vb_ = (const char*)Vh + (size_t)(kt) * (64 * LDV * 2); sv0 = *(const bf16x8*)(vb_ + voff0); sv1 = *(const bf16x8*)(vb_ + voff1); sv2 = *(const bf16x8*)(vb_ + voff0 + 256); sv3 = *(const bf16x8*)(vb_ + voff1 + 256); } while (0)
; #define ELOADK(kt) do { const char* kb_ = (const char*)Kh + (size_t)(kt) * (64 * LDK * 2); sk0 = *(const bf16x8*)(kb_ + koff0); sk1 = *(const bf16x8*)(kb_ + koff1); } while (0)
; #define EWRITEV(b) do { char* d_ = V_lds + (b) * D16_V; *(bf16x8*)(d_ + vst0) = sv0; *(bf16x8*)(d_ + vst1) = sv1; *(bf16x8*)(d_ + 8 * VP16 + vst0) = sv2; *(bf16x8*)(d_ + 8 * VP16 + vst1) = sv3; } while (0)
; #define EWRITEK(b) do { char* d_ = K_lds + (b) * PB_K; *(bf16x8*)(d_ + KSWZ(sr, sc * 2)) = sk0; *(bf16x8*)(d_ + KSWZ(32 + sr, sc * 2)) = sk1; } while (0)
; template <int LDQ, int LDK, int LDV, int LDO, int DMX> ...
;     ...
;     asm volatile("s_waitcnt vmcnt(0)" ::: "memory");
;     if (t + 2 < NT) EWRITEK(t & 1);
;     if (t + 1 < NT) EWRITEV((t + 1) & 1);
;     ELOADK(t + 3); ELOADV(t + 2);
;     SBAR(); pv16d<4>(o, vbo, vbp, pc, pp); SBAR();
;     if (more) ESM((t + 1) & 1);
.Lvd_kskip:
	v_lshl_add_u64 v[240:241], v[176:177], 0, s[6:7]
	v_add_co_u32_e32 v242, vcc, s41, v240
	s_nop 1
	v_addc_co_u32_e32 v243, vcc, 0, v241, vcc
	v_add_co_u32_e32 v240, vcc, s42, v240
	s_nop 1
	v_addc_co_u32_e32 v241, vcc, 0, v241, vcc
	global_load_dwordx4 v[52:55], v[242:243], off offset:1024
	global_load_dwordx4 v[56:59], v[240:241], off offset:1024
	s_add_u32 s6, s6, 0xc0000
	s_addc_u32 s7, s7, 0
	s_waitcnt lgkmcnt(4)
	s_nop 0
	v_mfma_f32_16x16x32_bf16 v[84:87], v[36:39], v[64:67], v[84:87]
	v_exp_f32_e32 v144, v144
	v_mfma_f32_16x16x32_bf16 v[92:95], v[36:39], v[68:71], v[92:95]
	v_exp_f32_e32 v240, v145
	v_mfma_f32_16x16x32_bf16 v[88:91], v[44:47], v[64:67], v[88:91]
	v_exp_f32_e32 v146, v146
	v_mfma_f32_16x16x32_bf16 v[96:99], v[44:47], v[68:71], v[96:99]
	v_exp_f32_e32 v242, v147
	v_mfma_f32_16x16x32_bf16 v[84:87], v[40:43], v[148:151], v[84:87]
	v_exp_f32_e32 v145, v140
	v_mfma_f32_16x16x32_bf16 v[92:95], v[40:43], v[152:155], v[92:95]
	v_exp_f32_e32 v241, v141
	v_mfma_f32_16x16x32_bf16 v[88:91], v[48:51], v[148:151], v[88:91]
	v_exp_f32_e32 v147, v142
	v_mfma_f32_16x16x32_bf16 v[96:99], v[48:51], v[152:155], v[96:99]
	v_exp_f32_e32 v243, v143
	ds_read_b64_tr_b16 v[180:181], v179 offset:0x38e0
	ds_read_b64_tr_b16 v[182:183], v179 offset:0x3ae0
	ds_read_b64_tr_b16 v[204:205], v178 offset:0x38e0
	ds_read_b64_tr_b16 v[206:207], v178 offset:0x3ae0
	s_waitcnt lgkmcnt(4)
	v_mfma_f32_16x16x32_bf16 v[60:63], v[232:235], v[64:67], v[60:63]
	s_add_i32 s55, s55, 1
	s_add_i32 s60, s55, -1
	s_and_b32 s57, s60, 1
	v_exp_f32_e32 v136, v136
	s_waitcnt lgkmcnt(0)
	v_mfma_f32_16x16x32_bf16 v[80:83], v[232:235], v[68:71], v[80:83]
	s_bitcmp1_b32 s55, 0
	s_cselect_b64 s[22:23], -1, 0
	s_and_b64 s[58:59], s[22:23], exec
	v_exp_f32_e32 v140, v137
	v_mfma_f32_16x16x32_bf16 v[60:63], v[236:239], v[148:151], v[60:63]
	s_cselect_b32 s58, 0x4400, 0
	s_cselect_b32 s85, 0x8200, 0
	v_exp_f32_e32 v138, v138
	v_mfma_f32_16x16x32_bf16 v[80:83], v[236:239], v[152:155], v[80:83]
	s_add_i32 s85, s85, s84
	v_add_u32_e32 v178, s58, v193
	v_exp_f32_e32 v142, v139
	v_mfma_f32_16x16x32_bf16 v[64:67], v[180:183], v[64:67], v[72:75]
	v_exp_f32_e32 v137, v132
	v_mfma_f32_16x16x32_bf16 v[68:71], v[180:183], v[68:71], v[76:79]
	v_exp_f32_e32 v141, v133
	v_mfma_f32_16x16x32_bf16 v[72:75], v[204:207], v[148:151], v[64:67]
	v_exp_f32_e32 v139, v134
	v_mfma_f32_16x16x32_bf16 v[76:79], v[204:207], v[152:155], v[68:71]
	v_exp_f32_e32 v143, v135
	s_nop 4
	s_and_b32 s22, s56, 0x4000
	v_add_u32_e32 v132, s22, v190
	v_cvt_pk_bf16_f32 v64, v144, v240
	v_cvt_pk_bf16_f32 v65, v146, v242
	v_cvt_pk_bf16_f32 v66, v136, v140
	v_cvt_pk_bf16_f32 v67, v138, v142
	v_cvt_pk_bf16_f32 v68, v145, v241
	v_cvt_pk_bf16_f32 v69, v147, v243
	v_cvt_pk_bf16_f32 v70, v137, v141
	v_cvt_pk_bf16_f32 v71, v139, v143
	ds_write_b128 v132, v[64:67]
	ds_write_b128 v132, v[68:71] offset:1024
	v_pk_add_f32 v[132:133], v[144:145], v[240:241]
	v_pk_add_f32 v[134:135], v[146:147], v[242:243]
	v_pk_add_f32 v[132:133], v[132:133], v[134:135]
	v_pk_add_f32 v[134:135], v[136:137], v[140:141]
	v_pk_add_f32 v[136:137], v[138:139], v[142:143]
	v_pk_add_f32 v[134:135], v[134:135], v[136:137]
	v_pk_add_f32 v[132:133], v[132:133], v[134:135]
	s_addk_i32 s56, 0x4000
	s_cmp_eq_u32 s6, 0xc240000
	v_pk_add_f32 v[174:175], v[174:175], v[132:133]
	s_cbranch_scc0 .LBB0_1271
